# v67 + same self-row de-serialisation for the second node group of k_agg1g2
# baseline (speedup 1.0000x reference)
.LBB2_12:
	s_or_b64 exec, exec, s[10:11]
	v_mov_b32_e32 v106, 0
	v_mov_b32_e32 v107, 0
	v_mov_b32_e32 v98, 0
	v_mov_b32_e32 v99, 0
	v_mov_b32_e32 v96, 0
	v_mov_b32_e32 v97, 0
	v_mov_b32_e32 v82, 0
	v_mov_b32_e32 v83, 0
	s_and_saveexec_b64 s[10:11], s[30:31]
	s_cbranch_execz .LBB2_14
	s_waitcnt lgkmcnt(7)
	v_lshl_add_u64 v[102:103], v[80:81], 0, v[66:67]
	s_waitcnt lgkmcnt(6)
	global_load_dwordx4 v[102:105], v[102:103], off
.LBB2_14:
	s_or_b64 exec, exec, s[10:11]
	s_waitcnt lgkmcnt(7)
	ds_read2_b32 v[10:11], v51 offset0:64 offset1:68
	s_waitcnt lgkmcnt(7)
	ds_read2_b32 v[12:13], v51 offset0:72 offset1:76
	s_waitcnt lgkmcnt(7)
	ds_read2_b32 v[14:15], v51 offset0:96 offset1:100
	s_waitcnt lgkmcnt(2)
	v_lshl_add_u32 v10, v10, 7, v110
	global_load_dwordx4 v[46:49], v10, s[34:35]
	v_lshl_add_u32 v10, v11, 7, v110
	global_load_dwordx4 v[42:45], v10, s[34:35]
	s_waitcnt lgkmcnt(1)
	v_lshl_add_u32 v10, v12, 7, v110
	global_load_dwordx4 v[34:37], v10, s[34:35]
	v_lshl_add_u32 v10, v13, 7, v110
	global_load_dwordx4 v[38:41], v10, s[34:35]
	ds_read2_b32 v[10:11], v51 offset0:80 offset1:84
	s_waitcnt lgkmcnt(0)
	v_lshl_add_u32 v10, v10, 7, v110
	global_load_dwordx4 v[26:29], v10, s[34:35]
	v_lshl_add_u32 v10, v11, 7, v110
	global_load_dwordx4 v[30:33], v10, s[34:35]
	ds_read2_b32 v[10:11], v51 offset0:88 offset1:92
	s_waitcnt lgkmcnt(0)
	v_lshl_add_u32 v10, v10, 7, v110
	global_load_dwordx4 v[22:25], v10, s[34:35]
	v_lshl_add_u32 v10, v11, 7, v110
	global_load_dwordx4 v[18:21], v10, s[34:35]
	v_lshl_add_u32 v10, v14, 7, v110
	global_load_dwordx4 v[10:13], v10, s[34:35]
	v_lshl_add_u32 v14, v15, 7, v110
	global_load_dwordx4 v[14:17], v14, s[34:35]
	s_and_saveexec_b64 s[10:11], s[30:31]
	s_waitcnt vmcnt(10)
	v_fma_mix_f32 v82, v78, v105, 0 op_sel_hi:[0,1,0]
	v_fma_mix_f32 v83, v79, v105, 0 op_sel:[0,1,0] op_sel_hi:[0,1,0]
	v_fma_mix_f32 v96, v76, v104, 0 op_sel_hi:[0,1,0]
	v_fma_mix_f32 v97, v77, v104, 0 op_sel:[0,1,0] op_sel_hi:[0,1,0]
	v_fma_mix_f32 v98, v74, v103, 0 op_sel_hi:[0,1,0]
	v_fma_mix_f32 v99, v75, v103, 0 op_sel:[0,1,0] op_sel_hi:[0,1,0]
	v_fma_mix_f32 v106, v54, v102, 0 op_sel_hi:[0,1,0]
	v_fma_mix_f32 v107, v55, v102, 0 op_sel:[0,1,0] op_sel_hi:[0,1,0]
	s_or_b64 exec, exec, s[10:11]
	ds_read2_b32 v[104:105], v114 offset0:64 offset1:68
	ds_read2_b32 v[102:103], v114 offset0:72 offset1:76
	s_waitcnt lgkmcnt(1)
	v_mov_b32_e32 v90, v105
	s_waitcnt lgkmcnt(0)
	v_mov_b32_e32 v100, v103
	v_mov_b32_e32 v101, v102
	v_mov_b32_e32 v91, v104
	s_waitcnt vmcnt(9)
	v_cvt_f32_f16_e32 v116, v46
	v_cvt_f32_f16_sdwa v117, v46 dst_sel:DWORD dst_unused:UNUSED_PAD src0_sel:WORD_1
	v_cvt_f32_f16_e32 v46, v47
	v_cvt_f32_f16_sdwa v47, v47 dst_sel:DWORD dst_unused:UNUSED_PAD src0_sel:WORD_1
	s_waitcnt vmcnt(7)
	v_cvt_f32_f16_sdwa v95, v37 dst_sel:DWORD dst_unused:UNUSED_PAD src0_sel:WORD_1
	v_pk_fma_f32 v[106:107], v[104:105], v[116:117], v[106:107] op_sel_hi:[0,1,1]
	v_cvt_f32_f16_e32 v116, v42
	v_cvt_f32_f16_sdwa v117, v42 dst_sel:DWORD dst_unused:UNUSED_PAD src0_sel:WORD_1
	v_mov_b32_e32 v42, v105
	v_pk_fma_f32 v[46:47], v[104:105], v[46:47], v[98:99] op_sel_hi:[0,1,1]
	v_cvt_f32_f16_e32 v98, v43
	v_pk_fma_f32 v[106:107], v[42:43], v[116:117], v[106:107] op_sel_hi:[0,1,1]
	v_cvt_f32_f16_e32 v116, v34
	v_cvt_f32_f16_sdwa v117, v34 dst_sel:DWORD dst_unused:UNUSED_PAD src0_sel:WORD_1
	v_cvt_f32_f16_sdwa v99, v43 dst_sel:DWORD dst_unused:UNUSED_PAD src0_sel:WORD_1
	s_waitcnt vmcnt(6)
	v_cvt_f32_f16_sdwa v94, v41 dst_sel:DWORD dst_unused:UNUSED_PAD src0_sel:WORD_1
	v_mov_b32_e32 v34, v103
	v_pk_fma_f32 v[106:107], v[102:103], v[116:117], v[106:107] op_sel_hi:[0,1,1]
	v_cvt_f32_f16_e32 v116, v38
	v_cvt_f32_f16_sdwa v117, v38 dst_sel:DWORD dst_unused:UNUSED_PAD src0_sel:WORD_1
	v_pk_fma_f32 v[46:47], v[42:43], v[98:99], v[46:47] op_sel_hi:[0,1,1]
	v_cvt_f32_f16_e32 v98, v35
	v_cvt_f32_f16_sdwa v99, v35 dst_sel:DWORD dst_unused:UNUSED_PAD src0_sel:WORD_1
	v_pk_mul_f32 v[94:95], v[100:101], v[94:95]
	ds_read2_b32 v[100:101], v114 offset0:80 offset1:84
	v_cvt_f32_f16_e32 v38, v39
	v_cvt_f32_f16_sdwa v39, v39 dst_sel:DWORD dst_unused:UNUSED_PAD src0_sel:WORD_1
	v_pk_fma_f32 v[106:107], v[34:35], v[116:117], v[106:107] op_sel_hi:[0,1,1]
	s_waitcnt vmcnt(5)
	v_cvt_f32_f16_e32 v116, v26
	v_cvt_f32_f16_sdwa v117, v26 dst_sel:DWORD dst_unused:UNUSED_PAD src0_sel:WORD_1
	v_cvt_f32_f16_e32 v26, v27
	v_cvt_f32_f16_sdwa v27, v27 dst_sel:DWORD dst_unused:UNUSED_PAD src0_sel:WORD_1
	v_pk_fma_f32 v[46:47], v[102:103], v[98:99], v[46:47] op_sel_hi:[0,1,1]
	v_pk_fma_f32 v[38:39], v[34:35], v[38:39], v[46:47] op_sel_hi:[0,1,1]
	v_cvt_f32_f16_e32 v46, v44
	s_waitcnt lgkmcnt(0)
	v_pk_fma_f32 v[26:27], v[100:101], v[26:27], v[38:39] op_sel_hi:[0,1,1]
	v_cvt_f32_f16_e32 v38, v48
	v_cvt_f32_f16_sdwa v39, v48 dst_sel:DWORD dst_unused:UNUSED_PAD src0_sel:WORD_1
	v_cvt_f32_f16_sdwa v47, v44 dst_sel:DWORD dst_unused:UNUSED_PAD src0_sel:WORD_1
	v_cvt_f32_f16_e32 v60, v49
	v_cvt_f32_f16_sdwa v86, v45 dst_sel:DWORD dst_unused:UNUSED_PAD src0_sel:WORD_1
	v_pk_fma_f32 v[38:39], v[104:105], v[38:39], v[96:97] op_sel_hi:[0,1,1]
	v_pk_fma_f32 v[38:39], v[42:43], v[46:47], v[38:39] op_sel_hi:[0,1,1]
	v_cvt_f32_f16_e32 v42, v36
	v_cvt_f32_f16_sdwa v43, v36 dst_sel:DWORD dst_unused:UNUSED_PAD src0_sel:WORD_1
	v_mul_f32_e32 v88, v104, v60
	v_cvt_f32_f16_e32 v60, v45
	v_cvt_f32_f16_e32 v45, v37
	v_pk_fma_f32 v[36:37], v[102:103], v[42:43], v[38:39] op_sel_hi:[0,1,1]
	v_cvt_f32_f16_e32 v38, v40
	v_cvt_f32_f16_sdwa v39, v40 dst_sel:DWORD dst_unused:UNUSED_PAD src0_sel:WORD_1
	v_cvt_f32_f16_sdwa v87, v49 dst_sel:DWORD dst_unused:UNUSED_PAD src0_sel:WORD_1
	s_waitcnt vmcnt(4)
	v_cvt_f32_f16_e32 v96, v30
	v_cvt_f32_f16_sdwa v97, v30 dst_sel:DWORD dst_unused:UNUSED_PAD src0_sel:WORD_1
	v_pk_fma_f32 v[34:35], v[34:35], v[38:39], v[36:37] op_sel_hi:[0,1,1]
	v_cvt_f32_f16_e32 v36, v28
	v_cvt_f32_f16_sdwa v37, v28 dst_sel:DWORD dst_unused:UNUSED_PAD src0_sel:WORD_1
	v_cvt_f32_f16_e32 v28, v29
	v_cvt_f32_f16_sdwa v30, v33 dst_sel:DWORD dst_unused:UNUSED_PAD src0_sel:WORD_1
	v_pk_mul_f32 v[92:93], v[90:91], v[86:87]
	v_pk_fma_f32 v[38:39], v[100:101], v[36:37], v[34:35] op_sel_hi:[0,1,1]
	v_cvt_f32_f16_e32 v36, v31
	v_cvt_f32_f16_sdwa v37, v31 dst_sel:DWORD dst_unused:UNUSED_PAD src0_sel:WORD_1
	v_cvt_f32_f16_sdwa v31, v29 dst_sel:DWORD dst_unused:UNUSED_PAD src0_sel:WORD_1
	v_mul_f32_e32 v90, v102, v45
	v_cvt_f32_f16_e32 v45, v41
	v_mul_f32_e32 v34, v100, v28
	v_cvt_f32_f16_e32 v42, v32
	v_cvt_f32_f16_sdwa v43, v32 dst_sel:DWORD dst_unused:UNUSED_PAD src0_sel:WORD_1
	v_cvt_f32_f16_e32 v28, v33
	v_mov_b32_e32 v32, v101
	v_mov_b32_e32 v33, v100
	v_mov_b32_e32 v89, v93
	v_mul_f32_e32 v84, v105, v60
	v_pk_mul_f32 v[30:31], v[32:33], v[30:31]
	v_pk_add_f32 v[32:33], v[82:83], v[88:89]
	v_mov_b32_e32 v85, v92
	v_pk_add_f32 v[32:33], v[84:85], v[32:33]
	v_mov_b32_e32 v91, v95
	v_mul_f32_e32 v86, v103, v45
	v_pk_add_f32 v[32:33], v[90:91], v[32:33]
	v_mov_b32_e32 v87, v94
	v_pk_add_f32 v[32:33], v[86:87], v[32:33]
	v_mov_b32_e32 v35, v31
	ds_read2_b32 v[46:47], v114 offset0:88 offset1:92
	v_pk_add_f32 v[32:33], v[34:35], v[32:33]
	s_waitcnt vmcnt(3)
	v_cvt_f32_f16_e32 v34, v22
	v_cvt_f32_f16_sdwa v35, v22 dst_sel:DWORD dst_unused:UNUSED_PAD src0_sel:WORD_1
	v_pk_fma_f32 v[106:107], v[100:101], v[116:117], v[106:107] op_sel_hi:[0,1,1]
	v_mov_b32_e32 v40, v101
	v_pk_fma_f32 v[88:89], v[40:41], v[96:97], v[106:107] op_sel_hi:[0,1,1]
	s_waitcnt lgkmcnt(0)
	v_pk_fma_f32 v[34:35], v[46:47], v[34:35], v[88:89] op_sel_hi:[0,1,1]
	s_waitcnt vmcnt(2)
	v_cvt_f32_f16_e32 v88, v18
	v_cvt_f32_f16_sdwa v89, v18 dst_sel:DWORD dst_unused:UNUSED_PAD src0_sel:WORD_1
	v_cvt_f32_f16_e32 v84, v23
	v_cvt_f32_f16_sdwa v85, v23 dst_sel:DWORD dst_unused:UNUSED_PAD src0_sel:WORD_1
	ds_read2_b32 v[82:83], v114 offset0:96 offset1:100
	v_mov_b32_e32 v18, v47
	v_pk_fma_f32 v[26:27], v[40:41], v[36:37], v[26:27] op_sel_hi:[0,1,1]
	v_cvt_f32_f16_e32 v36, v19
	v_cvt_f32_f16_sdwa v37, v19 dst_sel:DWORD dst_unused:UNUSED_PAD src0_sel:WORD_1
	v_pk_fma_f32 v[34:35], v[18:19], v[88:89], v[34:35] op_sel_hi:[0,1,1]
	s_waitcnt vmcnt(1)
	v_cvt_f32_f16_e32 v88, v10
	v_cvt_f32_f16_sdwa v89, v10 dst_sel:DWORD dst_unused:UNUSED_PAD src0_sel:WORD_1
	v_pk_fma_f32 v[26:27], v[46:47], v[84:85], v[26:27] op_sel_hi:[0,1,1]
	v_pk_fma_f32 v[26:27], v[18:19], v[36:37], v[26:27] op_sel_hi:[0,1,1]
	v_cvt_f32_f16_e32 v36, v11
	v_cvt_f32_f16_sdwa v37, v11 dst_sel:DWORD dst_unused:UNUSED_PAD src0_sel:WORD_1
	s_waitcnt lgkmcnt(0)
	v_pk_fma_f32 v[34:35], v[82:83], v[88:89], v[34:35] op_sel_hi:[0,1,1]
	s_waitcnt vmcnt(0)
	v_cvt_f32_f16_e32 v88, v14
	v_cvt_f32_f16_sdwa v89, v14 dst_sel:DWORD dst_unused:UNUSED_PAD src0_sel:WORD_1
	v_cvt_f32_f16_e32 v14, v15
	v_cvt_f32_f16_sdwa v15, v15 dst_sel:DWORD dst_unused:UNUSED_PAD src0_sel:WORD_1
	v_cvt_f32_f16_e32 v86, v24
	v_cvt_f32_f16_sdwa v87, v24 dst_sel:DWORD dst_unused:UNUSED_PAD src0_sel:WORD_1
	v_mov_b32_e32 v10, v83
	v_pk_fma_f32 v[26:27], v[82:83], v[36:37], v[26:27] op_sel_hi:[0,1,1]
	v_pk_fma_f32 v[36:37], v[10:11], v[14:15], v[26:27] op_sel_hi:[0,1,1]
	v_cvt_f32_f16_e32 v26, v20
	v_cvt_f32_f16_sdwa v27, v20 dst_sel:DWORD dst_unused:UNUSED_PAD src0_sel:WORD_1
	v_pk_fma_f32 v[14:15], v[40:41], v[42:43], v[38:39] op_sel_hi:[0,1,1]
	v_pk_fma_f32 v[14:15], v[46:47], v[86:87], v[14:15] op_sel_hi:[0,1,1]
	v_cvt_f32_f16_sdwa v45, v25 dst_sel:DWORD dst_unused:UNUSED_PAD src0_sel:WORD_1
	v_pk_fma_f32 v[14:15], v[18:19], v[26:27], v[14:15] op_sel_hi:[0,1,1]
	v_cvt_f32_f16_e32 v18, v12
	v_cvt_f32_f16_sdwa v19, v12 dst_sel:DWORD dst_unused:UNUSED_PAD src0_sel:WORD_1
	v_cvt_f32_f16_sdwa v44, v21 dst_sel:DWORD dst_unused:UNUSED_PAD src0_sel:WORD_1
	v_cvt_f32_f16_e32 v22, v25
	v_cvt_f32_f16_e32 v23, v21
	v_pk_fma_f32 v[14:15], v[82:83], v[18:19], v[14:15] op_sel_hi:[0,1,1]
	v_cvt_f32_f16_e32 v18, v16
	v_cvt_f32_f16_sdwa v19, v16 dst_sel:DWORD dst_unused:UNUSED_PAD src0_sel:WORD_1
	v_cvt_f32_f16_e32 v21, v13
	v_cvt_f32_f16_sdwa v13, v13 dst_sel:DWORD dst_unused:UNUSED_PAD src0_sel:WORD_1
	v_cvt_f32_f16_sdwa v12, v17 dst_sel:DWORD dst_unused:UNUSED_PAD src0_sel:WORD_1
	v_mov_b32_e32 v48, v47
	v_mov_b32_e32 v49, v46
	v_mul_f32_e32 v28, v101, v28
	v_pk_mul_f32 v[44:45], v[48:49], v[44:45]
	v_pk_fma_f32 v[34:35], v[10:11], v[88:89], v[34:35] op_sel_hi:[0,1,1]
	v_pk_fma_f32 v[38:39], v[10:11], v[18:19], v[14:15] op_sel_hi:[0,1,1]
	v_cvt_f32_f16_e32 v10, v17
	v_mov_b32_e32 v14, v83
	v_mov_b32_e32 v15, v82
	v_mov_b32_e32 v29, v30
	v_mul_f32_e32 v22, v46, v22
	v_mul_f32_e32 v24, v47, v23
	v_pk_mul_f32 v[12:13], v[14:15], v[12:13]
	v_pk_add_f32 v[14:15], v[28:29], v[32:33]
	v_mov_b32_e32 v23, v45
	v_pk_add_f32 v[14:15], v[22:23], v[14:15]
	v_mov_b32_e32 v25, v44
	v_mul_f32_e32 v48, v82, v21
	v_pk_add_f32 v[14:15], v[24:25], v[14:15]
	v_mov_b32_e32 v49, v13
	v_mul_f32_e32 v10, v83, v10
	v_pk_add_f32 v[14:15], v[48:49], v[14:15]
	v_mov_b32_e32 v11, v12
	v_pk_add_f32 v[40:41], v[10:11], v[14:15]
	s_and_saveexec_b64 s[10:11], s[6:7]
	s_cbranch_execz .LBB2_16
	ds_read2_b32 v[10:11], v51 offset0:104 offset1:108
	ds_read2_b32 v[12:13], v51 offset0:112 offset1:116
	ds_read2_b32 v[14:15], v51 offset0:120 offset1:124
	s_waitcnt lgkmcnt(2)
	v_lshl_add_u32 v10, v10, 7, v110
	v_lshl_add_u32 v11, v11, 7, v110
	global_load_dwordx4 v[30:33], v10, s[34:35]
	global_load_dwordx4 v[26:29], v11, s[34:35]
	s_waitcnt lgkmcnt(1)
	v_lshl_add_u32 v10, v12, 7, v110
	v_lshl_add_u32 v11, v13, 7, v110
	global_load_dwordx4 v[22:25], v10, s[34:35]
	global_load_dwordx4 v[18:21], v11, s[34:35]
	s_waitcnt lgkmcnt(0)
	v_lshl_add_u32 v10, v14, 7, v110
	global_load_dwordx4 v[10:13], v10, s[34:35]
	v_lshl_add_u32 v14, v15, 7, v110
	global_load_dwordx4 v[14:17], v14, s[34:35]
	ds_read2_b32 v[44:45], v114 offset0:104 offset1:108
	ds_read2_b32 v[42:43], v114 offset0:112 offset1:116
	ds_read2_b32 v[46:47], v114 offset0:120 offset1:124
	s_waitcnt lgkmcnt(2)
	v_mov_b32_e32 v84, v45
	v_mov_b32_e32 v85, v44
	v_mov_b32_e32 v60, v45
	s_waitcnt lgkmcnt(1)
	v_mov_b32_e32 v82, v43
	v_mov_b32_e32 v83, v42
	v_mov_b32_e32 v86, v43
	s_waitcnt lgkmcnt(0)
	v_mov_b32_e32 v48, v47
	s_waitcnt vmcnt(5)
	v_cvt_f32_f16_e32 v92, v30
	v_cvt_f32_f16_sdwa v93, v30 dst_sel:DWORD dst_unused:UNUSED_PAD src0_sel:WORD_1
	v_cvt_f32_f16_e32 v30, v31
	v_cvt_f32_f16_sdwa v31, v31 dst_sel:DWORD dst_unused:UNUSED_PAD src0_sel:WORD_1
	v_cvt_f32_f16_e32 v104, v32
	v_cvt_f32_f16_sdwa v105, v32 dst_sel:DWORD dst_unused:UNUSED_PAD src0_sel:WORD_1
	v_cvt_f32_f16_e32 v49, v33
	v_cvt_f32_f16_sdwa v89, v33 dst_sel:DWORD dst_unused:UNUSED_PAD src0_sel:WORD_1
	s_waitcnt vmcnt(4)
	v_cvt_f32_f16_sdwa v88, v29 dst_sel:DWORD dst_unused:UNUSED_PAD src0_sel:WORD_1
	v_cvt_f32_f16_e32 v94, v26
	v_cvt_f32_f16_sdwa v95, v26 dst_sel:DWORD dst_unused:UNUSED_PAD src0_sel:WORD_1
	v_cvt_f32_f16_e32 v26, v27
	v_cvt_f32_f16_sdwa v27, v27 dst_sel:DWORD dst_unused:UNUSED_PAD src0_sel:WORD_1
	v_cvt_f32_f16_e32 v32, v28
	v_cvt_f32_f16_sdwa v33, v28 dst_sel:DWORD dst_unused:UNUSED_PAD src0_sel:WORD_1
	v_cvt_f32_f16_e32 v87, v29
	s_waitcnt vmcnt(3)
	v_cvt_f32_f16_e32 v96, v22
	v_cvt_f32_f16_sdwa v97, v22 dst_sel:DWORD dst_unused:UNUSED_PAD src0_sel:WORD_1
	v_cvt_f32_f16_e32 v22, v23
	v_cvt_f32_f16_sdwa v23, v23 dst_sel:DWORD dst_unused:UNUSED_PAD src0_sel:WORD_1
	v_cvt_f32_f16_e32 v28, v24
	v_cvt_f32_f16_sdwa v29, v24 dst_sel:DWORD dst_unused:UNUSED_PAD src0_sel:WORD_1
	v_cvt_f32_f16_e32 v117, v25
	v_cvt_f32_f16_sdwa v91, v25 dst_sel:DWORD dst_unused:UNUSED_PAD src0_sel:WORD_1
	s_waitcnt vmcnt(2)
	v_cvt_f32_f16_sdwa v90, v21 dst_sel:DWORD dst_unused:UNUSED_PAD src0_sel:WORD_1
	v_cvt_f32_f16_e32 v98, v18
	v_cvt_f32_f16_sdwa v99, v18 dst_sel:DWORD dst_unused:UNUSED_PAD src0_sel:WORD_1
	v_cvt_f32_f16_e32 v18, v19
	v_cvt_f32_f16_sdwa v19, v19 dst_sel:DWORD dst_unused:UNUSED_PAD src0_sel:WORD_1
	v_cvt_f32_f16_e32 v24, v20
	v_cvt_f32_f16_sdwa v25, v20 dst_sel:DWORD dst_unused:UNUSED_PAD src0_sel:WORD_1
	v_cvt_f32_f16_e32 v118, v21
	s_waitcnt vmcnt(1)
	v_cvt_f32_f16_e32 v100, v10
	v_cvt_f32_f16_sdwa v101, v10 dst_sel:DWORD dst_unused:UNUSED_PAD src0_sel:WORD_1
	v_cvt_f32_f16_e32 v10, v11
	v_cvt_f32_f16_sdwa v11, v11 dst_sel:DWORD dst_unused:UNUSED_PAD src0_sel:WORD_1
	v_cvt_f32_f16_e32 v20, v12
	v_cvt_f32_f16_sdwa v21, v12 dst_sel:DWORD dst_unused:UNUSED_PAD src0_sel:WORD_1
	v_pk_fma_f32 v[30:31], v[44:45], v[30:31], v[36:37] op_sel_hi:[0,1,1]
	v_pk_fma_f32 v[36:37], v[44:45], v[104:105], v[38:39] op_sel_hi:[0,1,1]
	v_cvt_f32_f16_e32 v119, v13
	v_cvt_f32_f16_sdwa v13, v13 dst_sel:DWORD dst_unused:UNUSED_PAD src0_sel:WORD_1
	s_waitcnt vmcnt(0)
	v_cvt_f32_f16_sdwa v12, v17 dst_sel:DWORD dst_unused:UNUSED_PAD src0_sel:WORD_1
	v_pk_mul_f32 v[84:85], v[84:85], v[88:89]
	v_pk_fma_f32 v[26:27], v[60:61], v[26:27], v[30:31] op_sel_hi:[0,1,1]
	v_pk_fma_f32 v[30:31], v[60:61], v[32:33], v[36:37] op_sel_hi:[0,1,1]
	v_cvt_f32_f16_e32 v106, v16
	v_cvt_f32_f16_sdwa v107, v16 dst_sel:DWORD dst_unused:UNUSED_PAD src0_sel:WORD_1
	v_cvt_f32_f16_e32 v120, v17
	v_mul_f32_e32 v16, v44, v49
	v_pk_fma_f32 v[22:23], v[42:43], v[22:23], v[26:27] op_sel_hi:[0,1,1]
	v_pk_fma_f32 v[26:27], v[42:43], v[28:29], v[30:31] op_sel_hi:[0,1,1]
	v_mov_b32_e32 v17, v85
	v_mul_f32_e32 v116, v45, v87
	v_mul_f32_e32 v88, v42, v117
	v_pk_mul_f32 v[82:83], v[82:83], v[90:91]
	v_pk_fma_f32 v[34:35], v[44:45], v[92:93], v[34:35] op_sel_hi:[0,1,1]
	v_pk_fma_f32 v[18:19], v[86:87], v[18:19], v[22:23] op_sel_hi:[0,1,1]
	v_pk_fma_f32 v[22:23], v[86:87], v[24:25], v[26:27] op_sel_hi:[0,1,1]
	v_pk_add_f32 v[16:17], v[40:41], v[16:17]
	v_mov_b32_e32 v117, v84
	v_cvt_f32_f16_e32 v102, v14
	v_cvt_f32_f16_sdwa v103, v14 dst_sel:DWORD dst_unused:UNUSED_PAD src0_sel:WORD_1
	v_cvt_f32_f16_e32 v14, v15
	v_cvt_f32_f16_sdwa v15, v15 dst_sel:DWORD dst_unused:UNUSED_PAD src0_sel:WORD_1
	v_pk_fma_f32 v[34:35], v[60:61], v[94:95], v[34:35] op_sel_hi:[0,1,1]
	v_pk_fma_f32 v[10:11], v[46:47], v[10:11], v[18:19] op_sel_hi:[0,1,1]
	v_pk_fma_f32 v[18:19], v[46:47], v[20:21], v[22:23] op_sel_hi:[0,1,1]
	v_mov_b32_e32 v22, v47
	v_mov_b32_e32 v23, v46
	v_pk_add_f32 v[16:17], v[116:117], v[16:17]
	v_mov_b32_e32 v89, v83
	v_mul_f32_e32 v118, v43, v118
	v_mul_f32_e32 v90, v46, v119
	v_pk_fma_f32 v[32:33], v[42:43], v[96:97], v[34:35] op_sel_hi:[0,1,1]
	v_pk_mul_f32 v[12:13], v[22:23], v[12:13]
	v_pk_add_f32 v[16:17], v[88:89], v[16:17]
	v_mov_b32_e32 v119, v82
	v_pk_fma_f32 v[28:29], v[86:87], v[98:99], v[32:33] op_sel_hi:[0,1,1]
	v_pk_add_f32 v[16:17], v[118:119], v[16:17]
	v_mov_b32_e32 v91, v13
	v_pk_fma_f32 v[24:25], v[46:47], v[100:101], v[28:29] op_sel_hi:[0,1,1]
	v_mul_f32_e32 v20, v47, v120
	v_pk_add_f32 v[16:17], v[90:91], v[16:17]
	v_mov_b32_e32 v21, v12
	v_pk_fma_f32 v[34:35], v[48:49], v[102:103], v[24:25] op_sel_hi:[0,1,1]
	v_pk_fma_f32 v[36:37], v[48:49], v[14:15], v[10:11] op_sel_hi:[0,1,1]
	v_pk_fma_f32 v[38:39], v[48:49], v[106:107], v[18:19] op_sel_hi:[0,1,1]
	v_pk_add_f32 v[40:41], v[20:21], v[16:17]
